# attention: last xor-32 bpermute -> permlane32 swap, dead lane-index ops removed (on v9)
# speedup vs baseline: 1.0037x; 1.0014x over previous
.LBB0_1238:
	s_mul_i32 s12, s36, 0x4800
	s_add_i32 s13, s12, 0xffffb800
	s_cmp_lg_u32 s36, 0
	s_cselect_b32 s13, s13, 0x9000
	s_add_i32 s13, s13, 0
	s_add_i32 s13, s13, 0x12c00
	s_add_u32 s16, s82, s2
	s_addc_u32 s17, s83, s3
	s_add_u32 s16, s16, s28
	s_addc_u32 s17, s17, s29
	s_add_i32 m0, s13, s69
	s_nop 0
	global_load_lds_dwordx4 v212, s[16:17]
	s_add_i32 m0, s13, s70
	s_nop 0
	global_load_lds_dwordx4 v213, s[16:17]
	s_add_i32 m0, s13, s71
	s_nop 0
	global_load_lds_dwordx4 v214, s[16:17]
	v_max_f32_e32 v82, v67, v67
	v_max_f32_e32 v83, v66, v66
	v_max_f32_e32 v82, v83, v82
	v_max3_f32 v82, v82, v68, v69
	v_max3_f32 v82, v82, v70, v71
	v_max3_f32 v82, v82, v72, v73
	v_max3_f32 v82, v82, v74, v75
	v_max3_f32 v82, v82, v76, v77
	v_max3_f32 v82, v82, v78, v79
	v_max3_f32 v82, v82, v80, v81
	v_mov_b32_e32 v83, v82
	s_nop 1
	v_permlane32_swap_b32_e32 v83, v82
	s_waitcnt lgkmcnt(0)
	v_max_f32_e32 v83, v83, v83
	v_max_f32_e32 v82, v82, v83
	v_add_f32_e32 v83, 0x41000000, v183
	v_cmp_gt_f32_e32 vcc, v82, v83
	s_cbranch_vccz .LBB0_1240
	v_max_f32_e32 v82, v82, v82
	v_max_f32_e32 v83, v183, v183
	v_max_f32_e32 v83, v83, v82
	v_sub_f32_e32 v82, v183, v83
	v_exp_f32_e32 v82, v82
	v_mov_b32_e32 v183, v83
	v_pk_mul_f32 v[64:65], v[64:65], v[82:83] op_sel_hi:[1,0]
	v_pk_mul_f32 v[62:63], v[62:63], v[82:83] op_sel_hi:[1,0]
	v_pk_mul_f32 v[60:61], v[60:61], v[82:83] op_sel_hi:[1,0]
	v_pk_mul_f32 v[58:59], v[58:59], v[82:83] op_sel_hi:[1,0]
	v_pk_mul_f32 v[56:57], v[56:57], v[82:83] op_sel_hi:[1,0]
	v_pk_mul_f32 v[54:55], v[54:55], v[82:83] op_sel_hi:[1,0]
	v_pk_mul_f32 v[52:53], v[52:53], v[82:83] op_sel_hi:[1,0]
	v_pk_mul_f32 v[50:51], v[50:51], v[82:83] op_sel_hi:[1,0]
	v_pk_mul_f32 v[48:49], v[48:49], v[82:83] op_sel_hi:[1,0]
	v_pk_mul_f32 v[46:47], v[46:47], v[82:83] op_sel_hi:[1,0]
	v_pk_mul_f32 v[44:45], v[44:45], v[82:83] op_sel_hi:[1,0]
	v_pk_mul_f32 v[42:43], v[42:43], v[82:83] op_sel_hi:[1,0]
	v_pk_mul_f32 v[40:41], v[40:41], v[82:83] op_sel_hi:[1,0]
	v_pk_mul_f32 v[38:39], v[38:39], v[82:83] op_sel_hi:[1,0]
	v_pk_mul_f32 v[36:37], v[36:37], v[82:83] op_sel_hi:[1,0]
	v_pk_mul_f32 v[34:35], v[34:35], v[82:83] op_sel_hi:[1,0]
	v_pk_mul_f32 v[32:33], v[32:33], v[82:83] op_sel_hi:[1,0]
	v_pk_mul_f32 v[30:31], v[30:31], v[82:83] op_sel_hi:[1,0]
	v_pk_mul_f32 v[28:29], v[28:29], v[82:83] op_sel_hi:[1,0]
	v_pk_mul_f32 v[26:27], v[26:27], v[82:83] op_sel_hi:[1,0]
	v_pk_mul_f32 v[24:25], v[24:25], v[82:83] op_sel_hi:[1,0]
	v_pk_mul_f32 v[22:23], v[22:23], v[82:83] op_sel_hi:[1,0]
	v_pk_mul_f32 v[20:21], v[20:21], v[82:83] op_sel_hi:[1,0]
	v_pk_mul_f32 v[18:19], v[18:19], v[82:83] op_sel_hi:[1,0]
	v_pk_mul_f32 v[16:17], v[16:17], v[82:83] op_sel_hi:[1,0]
	v_pk_mul_f32 v[14:15], v[14:15], v[82:83] op_sel_hi:[1,0]
	v_pk_mul_f32 v[12:13], v[12:13], v[82:83] op_sel_hi:[1,0]
	v_pk_mul_f32 v[10:11], v[10:11], v[82:83] op_sel_hi:[1,0]
	v_pk_mul_f32 v[8:9], v[8:9], v[82:83] op_sel_hi:[1,0]
	v_pk_mul_f32 v[6:7], v[6:7], v[82:83] op_sel_hi:[1,0]
	v_pk_mul_f32 v[4:5], v[4:5], v[82:83] op_sel_hi:[1,0]
	v_pk_mul_f32 v[2:3], v[2:3], v[82:83] op_sel_hi:[1,0]
	v_mul_f32_e32 v186, v186, v82

.LBB0_1248:
	v_add_f32_e32 v66, 0, v66
	v_add_f32_e32 v66, v78, v66
	v_add_f32_e32 v66, v67, v66
	v_add_f32_e32 v66, v79, v66
	v_add_f32_e32 v66, v68, v66
	v_max_f32_e32 v67, v83, v83
	v_max_f32_e32 v68, v82, v82
	v_max_f32_e32 v67, v68, v67
	v_max3_f32 v67, v67, v84, v85
	v_add_f32_e32 v66, v80, v66
	v_max3_f32 v67, v67, v86, v87
	v_add_f32_e32 v66, v69, v66
	v_max3_f32 v67, v67, v88, v89
	v_add_f32_e32 v66, v81, v66
	v_max3_f32 v67, v67, v90, v91
	v_add_f32_e32 v66, v70, v66
	v_max3_f32 v67, v67, v92, v93
	v_add_f32_e32 v66, v71, v66
	v_max3_f32 v67, v67, v94, v95
	v_add_f32_e32 v66, v72, v66
	v_max3_f32 v67, v67, v96, v97
	v_add_f32_e32 v66, v73, v66
	v_mov_b32_e32 v68, v67
	s_nop 1
	v_permlane32_swap_b32_e32 v68, v67
	v_add_f32_e32 v66, v74, v66
	v_add_f32_e32 v66, v75, v66
	v_add_f32_e32 v66, v76, v66
	v_add_f32_e32 v66, v77, v66
	v_add_f32_e32 v164, v186, v66
	s_waitcnt lgkmcnt(0)
	v_max_f32_e32 v66, v68, v68
	v_max_f32_e32 v66, v67, v66
	v_add_f32_e32 v67, 0x41000000, v183
	v_cmp_gt_f32_e32 vcc, v66, v67
	s_cbranch_vccz .LBB0_1235
	v_max_f32_e32 v66, v66, v66
	v_max_f32_e32 v67, v183, v183
	v_max_f32_e32 v67, v67, v66
	v_sub_f32_e32 v66, v183, v67
	v_exp_f32_e32 v66, v66
	v_mov_b32_e32 v183, v67
	v_pk_mul_f32 v[64:65], v[64:65], v[66:67] op_sel_hi:[1,0]
	v_pk_mul_f32 v[62:63], v[62:63], v[66:67] op_sel_hi:[1,0]
	v_pk_mul_f32 v[60:61], v[60:61], v[66:67] op_sel_hi:[1,0]
	v_pk_mul_f32 v[58:59], v[58:59], v[66:67] op_sel_hi:[1,0]
	v_pk_mul_f32 v[56:57], v[56:57], v[66:67] op_sel_hi:[1,0]
	v_pk_mul_f32 v[54:55], v[54:55], v[66:67] op_sel_hi:[1,0]
	v_pk_mul_f32 v[52:53], v[52:53], v[66:67] op_sel_hi:[1,0]
	v_pk_mul_f32 v[50:51], v[50:51], v[66:67] op_sel_hi:[1,0]
	v_pk_mul_f32 v[48:49], v[48:49], v[66:67] op_sel_hi:[1,0]
	v_pk_mul_f32 v[46:47], v[46:47], v[66:67] op_sel_hi:[1,0]
	v_pk_mul_f32 v[44:45], v[44:45], v[66:67] op_sel_hi:[1,0]
	v_pk_mul_f32 v[42:43], v[42:43], v[66:67] op_sel_hi:[1,0]
	v_pk_mul_f32 v[40:41], v[40:41], v[66:67] op_sel_hi:[1,0]
	v_pk_mul_f32 v[38:39], v[38:39], v[66:67] op_sel_hi:[1,0]
	v_pk_mul_f32 v[36:37], v[36:37], v[66:67] op_sel_hi:[1,0]
	v_pk_mul_f32 v[34:35], v[34:35], v[66:67] op_sel_hi:[1,0]
	v_pk_mul_f32 v[32:33], v[32:33], v[66:67] op_sel_hi:[1,0]
	v_pk_mul_f32 v[30:31], v[30:31], v[66:67] op_sel_hi:[1,0]
	v_pk_mul_f32 v[28:29], v[28:29], v[66:67] op_sel_hi:[1,0]
	v_pk_mul_f32 v[26:27], v[26:27], v[66:67] op_sel_hi:[1,0]
	v_pk_mul_f32 v[24:25], v[24:25], v[66:67] op_sel_hi:[1,0]
	v_pk_mul_f32 v[22:23], v[22:23], v[66:67] op_sel_hi:[1,0]
	v_pk_mul_f32 v[20:21], v[20:21], v[66:67] op_sel_hi:[1,0]
	v_pk_mul_f32 v[18:19], v[18:19], v[66:67] op_sel_hi:[1,0]
	v_pk_mul_f32 v[16:17], v[16:17], v[66:67] op_sel_hi:[1,0]
	v_pk_mul_f32 v[14:15], v[14:15], v[66:67] op_sel_hi:[1,0]
	v_pk_mul_f32 v[12:13], v[12:13], v[66:67] op_sel_hi:[1,0]
	v_pk_mul_f32 v[10:11], v[10:11], v[66:67] op_sel_hi:[1,0]
	v_pk_mul_f32 v[8:9], v[8:9], v[66:67] op_sel_hi:[1,0]
	v_pk_mul_f32 v[6:7], v[6:7], v[66:67] op_sel_hi:[1,0]
	v_pk_mul_f32 v[4:5], v[4:5], v[66:67] op_sel_hi:[1,0]
	v_pk_mul_f32 v[2:3], v[2:3], v[66:67] op_sel_hi:[1,0]
	v_mul_f32_e32 v164, v164, v66
	s_branch .LBB0_1235
